# HGRN2 chunk loop: counted vmcnt so this chunk's v values no longer wait for the next chunk's q/f prefetch and the previous chunk's output stores
# baseline (speedup 1.0000x reference)
.LBB0_295:
	s_waitcnt lgkmcnt(5)
	s_nop 9
	v_pk_mul_f32 v[4:5], v[4:5], v[60:61]
	s_waitcnt lgkmcnt(4)
	v_pk_mul_f32 v[8:9], v[8:9], v[56:57]
	s_waitcnt lgkmcnt(2)
	v_pk_mul_f32 v[12:13], v[12:13], v[52:53]
	s_waitcnt lgkmcnt(0)
	v_pk_mul_f32 v[16:17], v[16:17], v[64:65]
	v_pk_mul_f32 v[2:3], v[2:3], v[58:59]
	v_pk_mul_f32 v[6:7], v[6:7], v[54:55]
	v_pk_mul_f32 v[10:11], v[10:11], v[50:51]
	v_pk_mul_f32 v[14:15], v[14:15], v[62:63]
	v_pk_fma_f32 v[98:99], v[98:99], v[48:49], v[16:17]
	v_pk_fma_f32 v[96:97], v[96:97], v[46:47], v[14:15]
	v_pk_fma_f32 v[94:95], v[94:95], v[44:45], v[12:13]
	v_pk_fma_f32 v[92:93], v[92:93], v[42:43], v[10:11]
	v_pk_fma_f32 v[90:91], v[90:91], v[40:41], v[8:9]
	v_pk_fma_f32 v[88:89], v[88:89], v[38:39], v[6:7]
	v_pk_fma_f32 v[86:87], v[86:87], v[36:37], v[4:5]
	v_pk_fma_f32 v[84:85], v[84:85], v[34:35], v[2:3]
	v_readfirstlane_b32 s98, v0
	s_cmp_lt_u32 s98, 0x80
	s_cbranch_scc1 .Lhg_b1
	s_waitcnt vmcnt(8)
	s_branch .Lhg_bd
.Lhg_b1:
	s_waitcnt vmcnt(24)
.Lhg_bd:
	s_cmpk_lg_i32 s79, 0x208
	v_mov_b32_e32 v3, v123
	v_mov_b32_e32 v12, v125
	v_mov_b32_e32 v13, v127
	v_mov_b32_e32 v14, v129
	v_mov_b32_e32 v15, v131
	v_mov_b32_e32 v17, v133
	v_mov_b32_e32 v18, v135
	v_mov_b32_e32 v19, v138
	v_mov_b32_e32 v5, v124
	v_mov_b32_e32 v6, v126
	v_mov_b32_e32 v7, v128
	v_mov_b32_e32 v8, v130
	v_mov_b32_e32 v9, v132
	v_mov_b32_e32 v10, v134
	v_mov_b32_e32 v11, v136
	v_mov_b32_e32 v16, v137
	s_mov_b32 s7, s79
	s_cbranch_scc0 .LBB0_293

.LBB0_300:
	v_readfirstlane_b32 s98, v0
	s_cmp_lt_u32 s98, 0x80
	s_cselect_b32 s98, 1, 0
	s_cmp_lg_u32 s7, 0
	s_cselect_b32 s99, s98, 0
	s_cmpk_lg_i32 s7, 0x207
	s_cselect_b32 s98, 1, 0
	s_add_i32 s99, s99, s98
	s_cmp_eq_u32 s99, 0
	s_cbranch_scc1 .Lhg_w0
	s_cmp_eq_u32 s99, 1
	s_cbranch_scc1 .Lhg_w1
	s_waitcnt vmcnt(32)
	s_branch .Lhg_wd
.Lhg_w1:
	s_waitcnt vmcnt(16)
	s_branch .Lhg_wd

.Lhg_wd:
	v_cndmask_b32_e64 v29, v29, v3, s[40:41]
	v_cndmask_b32_e64 v2, v29, v2, s[38:39]
	v_cndmask_b32_e64 v2, v2, 0, s[34:35]
	v_add_f32_e32 v28, v28, v2
	v_sub_f32_e32 v28, v28, v3
	v_exp_f32_e32 v29, v28
	v_exp_f32_e64 v28, -v28
	v_lshlrev_b32_e32 v5, 16, v5
	v_lshlrev_b32_e32 v30, 1, v4
	v_add_f32_e32 v27, v27, v2
	v_mul_f32_e32 v5, v29, v5
	v_mul_f32_e32 v26, v28, v26
	v_xor_b32_e32 v28, s58, v30
	v_sub_f32_e32 v27, v27, v3
	v_ashrrev_i32_e32 v4, 5, v4
	v_cvt_pk_bf16_f32 v5, v5, v26
	v_add_u32_e32 v28, s1, v28
	v_exp_f32_e32 v29, v27
	v_lshrrev_b32_e32 v26, 16, v5
	ds_write_b16 v28, v5
	ds_write_b16 v28, v26 offset:8192
	v_add_u32_e32 v5, s60, v4
	v_and_or_b32 v28, v30, 62, s61
	v_exp_f32_e64 v27, -v27
	v_lshl_or_b32 v5, v5, 9, v28
	v_lshlrev_b32_e32 v6, 16, v6
	v_add_u32_e32 v5, 0, v5
	ds_write_b16 v5, v26 offset:16384
	ds_write_b16 v5, v113 offset:24576
	v_mul_f32_e32 v6, v29, v6
	v_xor_b32_e32 v26, s84, v30
	v_mul_f32_e32 v24, v27, v24
	v_cvt_pk_bf16_f32 v6, v6, v24
	v_add_u32_e32 v26, s64, v26
	v_lshrrev_b32_e32 v24, 16, v6
	ds_write_b16 v26, v6
	ds_write_b16 v26, v24 offset:8192
	v_add_f32_e32 v6, v25, v2
	v_sub_f32_e32 v6, v6, v3
	v_exp_f32_e32 v25, v6
	v_exp_f32_e64 v6, -v6
	v_lshlrev_b32_e32 v7, 16, v7
	ds_write_b16 v5, v24 offset:16448
	ds_write_b16 v5, v114 offset:24640
	v_mul_f32_e32 v7, v25, v7
	v_mul_f32_e32 v6, v6, v22
	v_xor_b32_e32 v22, s85, v30
	v_cvt_pk_bf16_f32 v6, v7, v6
	v_add_u32_e32 v22, s65, v22
	v_lshrrev_b32_e32 v7, 16, v6
	ds_write_b16 v22, v6
	ds_write_b16 v22, v7 offset:8192
	v_add_f32_e32 v6, v23, v2
	v_sub_f32_e32 v6, v6, v3
	v_exp_f32_e32 v22, v6
	v_exp_f32_e64 v6, -v6
	v_lshlrev_b32_e32 v8, 16, v8
	ds_write_b16 v5, v7 offset:16512
	ds_write_b16 v5, v115 offset:24704
	v_mul_f32_e32 v7, v22, v8
	v_mul_f32_e32 v6, v6, v21
	v_xor_b32_e32 v8, s95, v30
	v_cvt_pk_bf16_f32 v6, v7, v6
	v_add_u32_e32 v8, s70, v8
	v_lshrrev_b32_e32 v7, 16, v6
	ds_write_b16 v8, v6
	ds_write_b16 v8, v7 offset:8192
	v_add_f32_e32 v6, v19, v2
	v_sub_f32_e32 v6, v6, v3
	v_exp_f32_e32 v8, v6
	v_exp_f32_e64 v6, -v6
	v_lshlrev_b32_e32 v9, 16, v9
	ds_write_b16 v5, v7 offset:16576
	ds_write_b16 v5, v116 offset:24768
	v_mul_f32_e32 v5, v8, v9
	v_xor_b32_e32 v7, s24, v30
	v_mul_f32_e32 v6, v6, v20
	v_cvt_pk_bf16_f32 v5, v5, v6
	v_add_u32_e32 v7, s71, v7
	v_lshrrev_b32_e32 v6, 16, v5
	ds_write_b16 v7, v5
	ds_write_b16 v7, v6 offset:8192
	v_add_f32_e32 v5, v18, v2
	v_sub_f32_e32 v5, v5, v3
	v_exp_f32_e32 v7, v5
	v_exp_f32_e64 v5, -v5
	v_add_u32_e32 v4, s66, v4
	v_lshl_or_b32 v4, v4, 9, v28
	v_lshlrev_b32_e32 v10, 16, v10
	v_add_u32_e32 v4, 0, v4
	ds_write_b16 v4, v6 offset:16384
	ds_write_b16 v4, v117 offset:24576
	v_mul_f32_e32 v6, v7, v10
	v_mul_f32_e32 v5, v5, v15
	v_xor_b32_e32 v7, s67, v30
	v_cvt_pk_bf16_f32 v5, v6, v5
	v_add_u32_e32 v7, s74, v7
	v_lshrrev_b32_e32 v6, 16, v5
	ds_write_b16 v7, v5
	ds_write_b16 v7, v6 offset:8192
	v_add_f32_e32 v5, v17, v2
	v_sub_f32_e32 v5, v5, v3
	v_exp_f32_e32 v7, v5
	v_exp_f32_e64 v5, -v5
	v_add_f32_e32 v2, v14, v2
	v_sub_f32_e32 v2, v2, v3
	v_exp_f32_e32 v3, v2
	v_exp_f32_e64 v2, -v2
	v_lshlrev_b32_e32 v11, 16, v11
	ds_write_b16 v4, v6 offset:16448
	ds_write_b16 v4, v118 offset:24640
	v_mul_f32_e32 v6, v7, v11
	v_mul_f32_e32 v5, v5, v13
	v_xor_b32_e32 v7, s4, v30
	v_cvt_pk_bf16_f32 v5, v6, v5
	v_add_u32_e32 v7, s75, v7
	v_lshlrev_b32_e32 v16, 16, v16
	v_lshrrev_b32_e32 v6, 16, v5
	ds_write_b16 v7, v5
	ds_write_b16 v7, v6 offset:8192
	v_mul_f32_e32 v2, v2, v12
	v_xor_b32_e32 v5, s5, v30
	v_mul_f32_e32 v3, v3, v16
	v_cvt_pk_bf16_f32 v2, v3, v2
	v_add_u32_e32 v5, s78, v5
	s_andn2_b64 vcc, exec, s[76:77]
	ds_write_b16 v4, v6 offset:16512
	ds_write_b16 v4, v119 offset:24704
	v_lshrrev_b32_e32 v3, 16, v2
	ds_write_b16 v5, v2
	ds_write_b16 v5, v3 offset:8192
	ds_write_b16 v4, v3 offset:16576
	ds_write_b16 v4, v120 offset:24768
	s_cbranch_vccnz .LBB0_302
	s_mov_b32 s56, s79
	s_lshl_b32 s57, s56, 5
	s_cmp_gt_i32 s56, 7
	s_cselect_b32 s56, s90, 0xff
	s_sub_i32 s56, s56, s57
	s_and_b64 s[76:77], s[10:11], exec
	s_cselect_b32 s56, s57, s56
	s_add_i32 s56, s56, s6
	v_mad_i64_i32 v[2:3], s[76:77], s56, v224, v[82:83]
	s_add_i32 s56, s56, s0
	global_load_ushort v113, v[2:3], off
	v_mad_i64_i32 v[2:3], s[76:77], s56, v224, v[82:83]
	s_add_i32 s56, s56, s0
	global_load_ushort v114, v[2:3], off
	v_mad_i64_i32 v[2:3], s[76:77], s56, v224, v[82:83]
	s_add_i32 s56, s56, s0
	global_load_ushort v115, v[2:3], off
	v_mad_i64_i32 v[2:3], s[76:77], s56, v224, v[82:83]
	s_add_i32 s56, s56, s0
	global_load_ushort v116, v[2:3], off
	v_mad_i64_i32 v[2:3], s[76:77], s56, v224, v[82:83]
	s_add_i32 s56, s56, s0
	global_load_ushort v117, v[2:3], off
	v_mad_i64_i32 v[2:3], s[76:77], s56, v224, v[82:83]
	s_add_i32 s56, s56, s0
	global_load_ushort v118, v[2:3], off
	v_mad_i64_i32 v[2:3], s[76:77], s56, v224, v[82:83]
	s_add_i32 s56, s56, s0
	global_load_ushort v119, v[2:3], off
	v_mad_i64_i32 v[2:3], s[76:77], s56, v224, v[82:83]
	global_load_ushort v120, v[2:3], off
